# index_scores tile loop: MFMAs of the next head group issued among the weighted-relu FMAs of the current group (second bank of result registers), MFMA-to-VALU wait-state padding gone
# speedup vs baseline: 1.0022x; 1.0022x over previous
.LBB0_441:
	v_mfma_f32_16x16x32_bf16 v[110:113], v[74:77], v[62:65], 0
	s_add_i32 s19, s19, 8
	s_min_i32 s20, s19, s7
	s_lshl_b32 s20, s20, 11
	v_mfma_f32_16x16x32_bf16 v[114:117], v[74:77], v[4:7], 0
	v_add_u32_e32 v106, s20, v104
	v_add_u32_e32 v107, s20, v105
	global_load_dwordx4 v[132:135], v107, s[2:3]
	global_load_dwordx4 v[136:139], v106, s[2:3]
	s_add_i32 s20, s18, 0x80
	v_mfma_f32_16x16x32_bf16 v[110:113], v[70:73], v[0:3], v[110:113]
	s_cmp_ge_i32 s19, s6
	v_mfma_f32_16x16x32_bf16 v[114:117], v[70:73], v[8:11], v[114:117]
	v_mfma_f32_16x16x32_bf16 v[120:123], v[74:77], v[12:15], 0
	v_mfma_f32_16x16x32_bf16 v[124:127], v[74:77], v[20:23], 0
	v_mfma_f32_16x16x32_bf16 v[120:123], v[70:73], v[16:19], v[120:123]
	v_mfma_f32_16x16x32_bf16 v[124:127], v[70:73], v[24:27], v[124:127]
	v_mfma_f32_16x16x32_bf16 v[128:131], v[74:77], v[28:31], 0
	v_mfma_f32_16x16x32_bf16 v[208:211], v[74:77], v[42:45], 0
	v_mfma_f32_16x16x32_bf16 v[212:215], v[74:77], v[50:53], 0
	v_fma_f32 v88, v82, v110, 0
	v_fma_f32 v89, v82, v111, 0
	v_fma_f32 v108, v82, v112, 0
	v_fma_f32 v109, v82, v113, 0
	v_mfma_f32_16x16x32_bf16 v[216:219], v[74:77], v[58:61], 0
	v_fma_f32 v88, v82, |v110|, v88
	v_fma_f32 v89, v82, |v111|, v89
	v_fma_f32 v108, v82, |v112|, v108
	v_fma_f32 v109, v82, |v113|, v109
	v_mfma_f32_16x16x32_bf16 v[128:131], v[70:73], v[38:41], v[128:131]
	v_fmac_f32_e32 v88, v83, v114
	v_fmac_f32_e32 v89, v83, v115
	v_fmac_f32_e32 v108, v83, v116
	v_fmac_f32_e32 v109, v83, v117
	v_mfma_f32_16x16x32_bf16 v[208:211], v[70:73], v[46:49], v[208:211]
	v_fma_f32 v88, v83, |v114|, v88
	v_fma_f32 v89, v83, |v115|, v89
	v_fma_f32 v108, v83, |v116|, v108
	v_fma_f32 v109, v83, |v117|, v109
	v_mfma_f32_16x16x32_bf16 v[212:215], v[70:73], v[54:57], v[212:215]
	v_fmac_f32_e32 v88, v84, v120
	v_fmac_f32_e32 v89, v84, v121
	v_fmac_f32_e32 v108, v84, v122
	v_fmac_f32_e32 v109, v84, v123
	v_mfma_f32_16x16x32_bf16 v[216:219], v[70:73], v[66:69], v[216:219]
	v_fma_f32 v88, v84, |v120|, v88
	v_fma_f32 v89, v84, |v121|, v89
	v_fma_f32 v108, v84, |v122|, v108
	v_fma_f32 v109, v84, |v123|, v109
	v_fmac_f32_e32 v88, v85, v124
	v_fmac_f32_e32 v89, v85, v125
	v_fmac_f32_e32 v108, v85, v126
	v_fmac_f32_e32 v109, v85, v127
	v_fma_f32 v88, v85, |v124|, v88
	v_fma_f32 v89, v85, |v125|, v89
	v_fma_f32 v108, v85, |v126|, v108
	v_fma_f32 v109, v85, |v127|, v109
	v_mfma_f32_16x16x32_bf16 v[110:113], v[74:77], v[140:143], 0
	v_mfma_f32_16x16x32_bf16 v[114:117], v[74:77], v[148:151], 0
	v_mfma_f32_16x16x32_bf16 v[120:123], v[74:77], v[156:159], 0
	v_fmac_f32_e32 v88, v78, v128
	v_fmac_f32_e32 v89, v78, v129
	v_fmac_f32_e32 v108, v78, v130
	v_fmac_f32_e32 v109, v78, v131
	v_mfma_f32_16x16x32_bf16 v[124:127], v[74:77], v[164:167], 0
	v_fma_f32 v88, v78, |v128|, v88
	v_fma_f32 v89, v78, |v129|, v89
	v_fma_f32 v108, v78, |v130|, v108
	v_fma_f32 v109, v78, |v131|, v109
	v_mfma_f32_16x16x32_bf16 v[110:113], v[70:73], v[144:147], v[110:113]
	v_fmac_f32_e32 v88, v79, v208
	v_fmac_f32_e32 v89, v79, v209
	v_fmac_f32_e32 v108, v79, v210
	v_fmac_f32_e32 v109, v79, v211
	v_mfma_f32_16x16x32_bf16 v[114:117], v[70:73], v[152:155], v[114:117]
	v_fma_f32 v88, v79, |v208|, v88
	v_fma_f32 v89, v79, |v209|, v89
	v_fma_f32 v108, v79, |v210|, v108
	v_fma_f32 v109, v79, |v211|, v109
	v_mfma_f32_16x16x32_bf16 v[120:123], v[70:73], v[160:163], v[120:123]
	v_fmac_f32_e32 v88, v80, v212
	v_fmac_f32_e32 v89, v80, v213
	v_fmac_f32_e32 v108, v80, v214
	v_fmac_f32_e32 v109, v80, v215
	v_mfma_f32_16x16x32_bf16 v[124:127], v[70:73], v[168:171], v[124:127]
	v_fma_f32 v88, v80, |v212|, v88
	v_fma_f32 v89, v80, |v213|, v89
	v_fma_f32 v108, v80, |v214|, v108
	v_fma_f32 v109, v80, |v215|, v109
	v_fmac_f32_e32 v88, v81, v216
	v_fmac_f32_e32 v89, v81, v217
	v_fmac_f32_e32 v108, v81, v218
	v_fmac_f32_e32 v109, v81, v219
	v_fma_f32 v88, v81, |v216|, v88
	v_fma_f32 v89, v81, |v217|, v89
	v_fma_f32 v108, v81, |v218|, v108
	v_fma_f32 v109, v81, |v219|, v109
	v_mfma_f32_16x16x32_bf16 v[128:131], v[74:77], v[172:175], 0
	v_mfma_f32_16x16x32_bf16 v[208:211], v[74:77], v[180:183], 0
	v_mfma_f32_16x16x32_bf16 v[212:215], v[74:77], v[188:191], 0
	v_fmac_f32_e32 v88, v96, v110
	v_fmac_f32_e32 v89, v96, v111
	v_fmac_f32_e32 v108, v96, v112
	v_fmac_f32_e32 v109, v96, v113
	v_mfma_f32_16x16x32_bf16 v[216:219], v[74:77], v[196:199], 0
	v_fma_f32 v88, v96, |v110|, v88
	v_fma_f32 v89, v96, |v111|, v89
	v_fma_f32 v108, v96, |v112|, v108
	v_fma_f32 v109, v96, |v113|, v109
	v_mfma_f32_16x16x32_bf16 v[128:131], v[70:73], v[176:179], v[128:131]
	v_fmac_f32_e32 v88, v97, v114
	v_fmac_f32_e32 v89, v97, v115
	v_fmac_f32_e32 v108, v97, v116
	v_fmac_f32_e32 v109, v97, v117
	v_mfma_f32_16x16x32_bf16 v[208:211], v[70:73], v[184:187], v[208:211]
	v_fma_f32 v88, v97, |v114|, v88
	v_fma_f32 v89, v97, |v115|, v89
	v_fma_f32 v108, v97, |v116|, v108
	v_fma_f32 v109, v97, |v117|, v109
	v_mfma_f32_16x16x32_bf16 v[212:215], v[70:73], v[192:195], v[212:215]
	v_fmac_f32_e32 v88, v98, v120
	v_fmac_f32_e32 v89, v98, v121
	v_fmac_f32_e32 v108, v98, v122
	v_fmac_f32_e32 v109, v98, v123
	v_mfma_f32_16x16x32_bf16 v[216:219], v[70:73], v[200:203], v[216:219]
	v_fma_f32 v88, v98, |v120|, v88
	v_fma_f32 v89, v98, |v121|, v89
	v_fma_f32 v108, v98, |v122|, v108
	v_fma_f32 v109, v98, |v123|, v109
	v_fmac_f32_e32 v88, v99, v124
	v_fmac_f32_e32 v89, v99, v125
	v_fmac_f32_e32 v108, v99, v126
	v_fmac_f32_e32 v109, v99, v127
	v_fma_f32 v88, v99, |v124|, v88
	v_fma_f32 v89, v99, |v125|, v89
	v_fma_f32 v108, v99, |v126|, v108
	v_fma_f32 v109, v99, |v127|, v109
	v_fmac_f32_e32 v88, v100, v128
	v_fmac_f32_e32 v89, v100, v129
	v_fmac_f32_e32 v108, v100, v130
	v_fmac_f32_e32 v109, v100, v131
	v_fma_f32 v88, v100, |v128|, v88
	v_fma_f32 v89, v100, |v129|, v89
	v_fma_f32 v108, v100, |v130|, v108
	v_fma_f32 v109, v100, |v131|, v109
	v_fmac_f32_e32 v88, v101, v208
	v_fmac_f32_e32 v89, v101, v209
	v_fmac_f32_e32 v108, v101, v210
	v_fmac_f32_e32 v109, v101, v211
	v_fma_f32 v88, v101, |v208|, v88
	v_fma_f32 v89, v101, |v209|, v89
	v_fma_f32 v108, v101, |v210|, v108
	v_fma_f32 v109, v101, |v211|, v109
	v_fmac_f32_e32 v88, v102, v212
	v_fmac_f32_e32 v89, v102, v213
	v_fmac_f32_e32 v108, v102, v214
	v_fmac_f32_e32 v109, v102, v215
	v_fma_f32 v88, v102, |v212|, v88
	v_fma_f32 v89, v102, |v213|, v89
	v_fma_f32 v108, v102, |v214|, v108
	v_fma_f32 v109, v102, |v215|, v109
	v_fmac_f32_e32 v88, v103, v216
	v_fmac_f32_e32 v89, v103, v217
	v_fmac_f32_e32 v108, v103, v218
	v_fmac_f32_e32 v109, v103, v219
	v_fma_f32 v88, v103, |v216|, v88
	v_fma_f32 v89, v103, |v217|, v89
	v_fma_f32 v108, v103, |v218|, v108
	v_fma_f32 v109, v103, |v219|, v109
	s_nop 0
	v_cvt_pk_f16_f32 v88, v88, v89
	v_cvt_pk_f16_f32 v89, v108, v109
	s_cbranch_scc1 .LBB0_443
	s_mov_b32 s21, s18
	s_branch .LBB0_439
